# baseline (speedup 1.0000x reference)
.LBB5_127:
	v_cndmask_b32_e64 v1, 0, v4, s[10:11]
	v_cndmask_b32_e64 v2, 0, v5, s[10:11]
	s_nop 0
	v_add_f32_dpp v1, v1, v1 quad_perm:[1,0,3,2] row_mask:0xf bank_mask:0xf bound_ctrl:1
	s_nop 1
	v_add_f32_dpp v1, v1, v1 quad_perm:[2,3,0,1] row_mask:0xf bank_mask:0xf bound_ctrl:1
	s_nop 1
	v_add_f32_dpp v1, v1, v1 row_half_mirror row_mask:0xf bank_mask:0xf bound_ctrl:1
	s_nop 1
	v_add_f32_dpp v1, v1, v1 row_mirror row_mask:0xf bank_mask:0xf bound_ctrl:1
	s_nop 0
	v_readlane_b32 s10, v1, 0
	v_readlane_b32 s28, v1, 16
	v_readlane_b32 s11, v1, 32
	v_readlane_b32 s29, v1, 48
	v_add_f32_dpp v1, v2, v2 quad_perm:[1,0,3,2] row_mask:0xf bank_mask:0xf bound_ctrl:1
	s_nop 1
	v_add_f32_dpp v1, v1, v1 quad_perm:[2,3,0,1] row_mask:0xf bank_mask:0xf bound_ctrl:1
	s_nop 1
	v_add_f32_dpp v1, v1, v1 row_half_mirror row_mask:0xf bank_mask:0xf bound_ctrl:1
	s_nop 1
	v_add_f32_dpp v1, v1, v1 row_mirror row_mask:0xf bank_mask:0xf bound_ctrl:1
	s_nop 0
	v_readlane_b32 s18, v1, 0
	v_readlane_b32 s30, v1, 16
	v_readlane_b32 s19, v1, 32
	v_readlane_b32 s31, v1, 48
	s_and_saveexec_b64 s[12:13], s[6:7]
	s_cbranch_execz .LBB5_129
	v_mov_b32_e32 v2, s30
	v_mov_b32_e32 v3, s31
	v_mov_b32_e32 v4, s28
	v_mov_b32_e32 v5, s29
	v_pk_add_f32 v[2:3], s[18:19], v[2:3]
	v_pk_add_f32 v[4:5], s[10:11], v[4:5]
	v_mov_b32_e32 v6, v2
	v_mov_b32_e32 v7, v4
	v_mov_b32_e32 v4, v3
	v_pk_add_f32 v[2:3], v[6:7], v[4:5]
	s_mov_b32 s10, 0x750547fe
	v_cvt_f64_f32_e32 v[4:5], v3
	v_cvt_f64_f32_e32 v[2:3], v2
	s_mov_b32 s11, 0x3ed1ca13
	v_mul_f64 v[2:3], v[2:3], s[10:11]
	v_mul_f64 v[4:5], v[4:5], s[10:11]
	v_fma_f64 v[2:3], -v[4:5], v[4:5], v[2:3]
	v_cvt_f32_f64_e32 v1, v[2:3]
	v_max_f32_e32 v1, 0, v1
	v_add_f32_e32 v1, 0x3727c5ac, v1
	v_rsq_f32_e32 v3, v1
	v_cvt_f32_f64_e32 v2, v[4:5]
	v_mov_b32_e32 v1, 0x23e90
	ds_write_b64 v1, v[2:3]

.LBB5_169:
	v_cndmask_b32_e64 v0, 0, v2, s[10:11]
	v_cndmask_b32_e64 v1, 0, v3, s[10:11]
	s_nop 0
	v_add_f32_dpp v0, v0, v0 quad_perm:[1,0,3,2] row_mask:0xf bank_mask:0xf bound_ctrl:1
	s_nop 1
	v_add_f32_dpp v0, v0, v0 quad_perm:[2,3,0,1] row_mask:0xf bank_mask:0xf bound_ctrl:1
	s_nop 1
	v_add_f32_dpp v0, v0, v0 row_half_mirror row_mask:0xf bank_mask:0xf bound_ctrl:1
	s_nop 1
	v_add_f32_dpp v0, v0, v0 row_mirror row_mask:0xf bank_mask:0xf bound_ctrl:1
	s_nop 0
	v_readlane_b32 s10, v0, 0
	v_readlane_b32 s18, v0, 16
	v_readlane_b32 s11, v0, 32
	v_readlane_b32 s19, v0, 48
	v_add_f32_dpp v0, v1, v1 quad_perm:[1,0,3,2] row_mask:0xf bank_mask:0xf bound_ctrl:1
	s_nop 1
	v_add_f32_dpp v0, v0, v0 quad_perm:[2,3,0,1] row_mask:0xf bank_mask:0xf bound_ctrl:1
	s_nop 1
	v_add_f32_dpp v0, v0, v0 row_half_mirror row_mask:0xf bank_mask:0xf bound_ctrl:1
	s_nop 1
	v_add_f32_dpp v0, v0, v0 row_mirror row_mask:0xf bank_mask:0xf bound_ctrl:1
	s_nop 0
	v_readlane_b32 s16, v0, 0
	v_readlane_b32 s24, v0, 16
	v_readlane_b32 s17, v0, 32
	v_readlane_b32 s25, v0, 48
	s_and_saveexec_b64 s[12:13], s[6:7]
	s_cbranch_execz .LBB5_171
	v_mov_b32_e32 v0, s24
	v_mov_b32_e32 v1, s25
	v_mov_b32_e32 v2, s18
	v_mov_b32_e32 v3, s19
	v_pk_add_f32 v[0:1], s[16:17], v[0:1]
	v_pk_add_f32 v[2:3], s[10:11], v[2:3]
	v_mov_b32_e32 v4, v0
	v_mov_b32_e32 v5, v2
	v_mov_b32_e32 v2, v1
	v_pk_add_f32 v[0:1], v[4:5], v[2:3]
	s_mov_b32 s10, 0x750547fe
	v_cvt_f64_f32_e32 v[2:3], v1
	v_cvt_f64_f32_e32 v[0:1], v0
	s_mov_b32 s11, 0x3ed1ca13
	v_mul_f64 v[0:1], v[0:1], s[10:11]
	v_mul_f64 v[2:3], v[2:3], s[10:11]
	v_fma_f64 v[0:1], -v[2:3], v[2:3], v[0:1]
	v_cvt_f32_f64_e32 v0, v[0:1]
	v_max_f32_e32 v0, 0, v0
	v_add_f32_e32 v0, 0x3727c5ac, v0
	v_rsq_f32_e32 v1, v0
	v_cvt_f32_f64_e32 v0, v[2:3]
	v_mov_b32_e32 v2, 0x23e90
	ds_write_b64 v2, v[0:1]

.LBB5_203:
	v_cndmask_b32_e64 v36, 0, v38, s[2:3]
	v_cndmask_b32_e64 v37, 0, v39, s[2:3]
	s_nop 0
	v_add_f32_dpp v36, v36, v36 quad_perm:[1,0,3,2] row_mask:0xf bank_mask:0xf bound_ctrl:1
	s_nop 1
	v_add_f32_dpp v36, v36, v36 quad_perm:[2,3,0,1] row_mask:0xf bank_mask:0xf bound_ctrl:1
	s_nop 1
	v_add_f32_dpp v36, v36, v36 row_half_mirror row_mask:0xf bank_mask:0xf bound_ctrl:1
	s_nop 1
	v_add_f32_dpp v36, v36, v36 row_mirror row_mask:0xf bank_mask:0xf bound_ctrl:1
	s_nop 0
	v_readlane_b32 s2, v36, 0
	v_readlane_b32 s10, v36, 16
	v_readlane_b32 s3, v36, 32
	v_readlane_b32 s11, v36, 48
	v_add_f32_dpp v36, v37, v37 quad_perm:[1,0,3,2] row_mask:0xf bank_mask:0xf bound_ctrl:1
	s_nop 1
	v_add_f32_dpp v36, v36, v36 quad_perm:[2,3,0,1] row_mask:0xf bank_mask:0xf bound_ctrl:1
	s_nop 1
	v_add_f32_dpp v36, v36, v36 row_half_mirror row_mask:0xf bank_mask:0xf bound_ctrl:1
	s_nop 1
	v_add_f32_dpp v36, v36, v36 row_mirror row_mask:0xf bank_mask:0xf bound_ctrl:1
	s_nop 0
	v_readlane_b32 s8, v36, 0
	v_readlane_b32 s12, v36, 16
	v_readlane_b32 s9, v36, 32
	v_readlane_b32 s13, v36, 48
	s_and_saveexec_b64 s[4:5], s[6:7]
	s_cbranch_execz .LBB5_205
	v_mov_b32_e32 v36, s12
	v_mov_b32_e32 v37, s13
	v_mov_b32_e32 v38, s10
	v_mov_b32_e32 v39, s11
	v_pk_add_f32 v[36:37], s[8:9], v[36:37]
	v_pk_add_f32 v[38:39], s[2:3], v[38:39]
	v_mov_b32_e32 v40, v36
	v_mov_b32_e32 v41, v38
	v_mov_b32_e32 v38, v37
	v_pk_add_f32 v[36:37], v[40:41], v[38:39]
	s_mov_b32 s2, 0x750547fe
	v_cvt_f64_f32_e32 v[38:39], v37
	v_cvt_f64_f32_e32 v[36:37], v36
	s_mov_b32 s3, 0x3ed1ca13
	v_mul_f64 v[36:37], v[36:37], s[2:3]
	v_mul_f64 v[38:39], v[38:39], s[2:3]
	v_fma_f64 v[36:37], -v[38:39], v[38:39], v[36:37]
	v_cvt_f32_f64_e32 v36, v[36:37]
	v_max_f32_e32 v36, 0, v36
	v_add_f32_e32 v36, 0x3727c5ac, v36
	v_rsq_f32_e32 v37, v36
	v_cvt_f32_f64_e32 v36, v[38:39]
	v_mov_b32_e32 v38, 0x23e90
	ds_write_b64 v38, v[36:37]
